# v040 + mLSTM gate scans (chunk-summary and output units) as six DPP ops each instead of six ds_bpermute round trips; wave max butterflies xor 1/2/4/8 via DPP
# speedup vs baseline: 1.0080x; 1.0080x over previous
; #define LAS __attribute__((address_space(3)))
; #define SHX(v, m) (((m) < 32) ? __int_as_float(__builtin_amdgcn_ds_swizzle(__float_as_int(v), ((((m) & 31) << 10) | 0x1f))) : shx32(v))
; __device__ __forceinline__ float shfl_up_l(float v, int off, int lane) { return __int_as_float(__builtin_amdgcn_ds_bpermute(((lane - off) & 63) << 2, __float_as_int(v))); }
; __device__ __forceinline__ float shfl_l(float v, int src) { return __int_as_float(__builtin_amdgcn_ds_bpermute(src << 2, __float_as_int(v))); }
; __device__ __forceinline__ void gate_scan(const LAS float* li, LAS float* lf, int dir, int lane, int (&pos)[2], float (&b)[2], float (&x)[2], float& g) {
;     pos[0] = dir ? 127 - 2 * lane : 2 * lane; pos[1] = dir ? 126 - 2 * lane : 2 * lane + 1;
;     const float f0 = lf[pos[0]], f1 = lf[pos[1]]; const float s1 = f0 + f1; float inc = s1;
; #pragma unroll
;     for (int off = 1; off < 64; off <<= 1) { const float y = shfl_up_l(inc, off, lane); if (lane >= off) inc += y; }
;     const float exc = inc - s1; b[0] = exc + f0; b[1] = exc + s1; g = shfl_l(inc, 63);
;     lf[pos[0]] = b[0]; lf[pos[1]] = b[1];
;     x[0] = li[pos[0]] - b[0]; x[1] = li[pos[1]] - b[1];
; }
; __device__ __forceinline__ void m1_unit(LAS unsigned char* L, int u, const bf16* z, const float* gates, const float* cw, float* cloc, float* nloc, float* mg, int tid_) {
;     ...
;     if (w < 2) {
;         const int dir = w; LAS float* li = ga + dir * 256; LAS float* lf = li + 128; LAS float* wo = ga + 512 + dir * 128;
;         int pos[2]; float bq[2], xq[2], g; gate_scan(li, lf, dir, lane, pos, bq, xq, g);
;         float a0 = g + xq[0], a1 = g + xq[1], m = fmaxf(a0, a1);
;         m = fmaxf(m, SHX(m, 1)); m = fmaxf(m, SHX(m, 2)); m = fmaxf(m, SHX(m, 4)); m = fmaxf(m, SHX(m, 8)); m = fmaxf(m, SHX(m, 16)); m = fmaxf(m, SHX(m, 32));
;         wo[pos[0]] = __expf(a0 - m); wo[pos[1]] = __expf(a1 - m);
;         if (lane == 0) { mg[((size_t)dir * 512 + u) * 2 + 0] = m; mg[((size_t)dir * 512 + u) * 2 + 1] = g; }
.LBB0_446:
	s_or_b64 exec, exec, s[8:9]
	v_ashrrev_i32_e32 v42, 1, v48
	v_ashrrev_i32_e32 v46, 6, v48
	v_and_b32_e32 v42, -2, v42
	v_mul_u32_u24_e32 v43, 0x110, v45
	v_and_b32_e32 v1, 63, v48
	v_add3_u32 v42, 0, v43, v42
	v_cmp_gt_i32_e32 vcc, 2, v46
	s_waitcnt vmcnt(5)
	ds_write_b16 v42, v38
	ds_write_b16_d16_hi v42, v38 offset:272
	ds_write_b16 v42, v39 offset:544
	ds_write_b16_d16_hi v42, v39 offset:816
	ds_write_b16 v42, v40 offset:1088
	ds_write_b16_d16_hi v42, v40 offset:1360
	ds_write_b16 v42, v41 offset:1632
	ds_write_b16_d16_hi v42, v41 offset:1904
	s_waitcnt vmcnt(4)
	ds_write_b16 v42, v34 offset:2176
	ds_write_b16_d16_hi v42, v34 offset:2448
	ds_write_b16 v42, v35 offset:2720
	ds_write_b16_d16_hi v42, v35 offset:2992
	ds_write_b16 v42, v36 offset:3264
	ds_write_b16_d16_hi v42, v36 offset:3536
	ds_write_b16 v42, v37 offset:3808
	ds_write_b16_d16_hi v42, v37 offset:4080
	s_waitcnt vmcnt(3)
	ds_write_b16 v42, v30 offset:4352
	ds_write_b16_d16_hi v42, v30 offset:4624
	ds_write_b16 v42, v31 offset:4896
	ds_write_b16_d16_hi v42, v31 offset:5168
	ds_write_b16 v42, v32 offset:5440
	ds_write_b16_d16_hi v42, v32 offset:5712
	ds_write_b16 v42, v33 offset:5984
	ds_write_b16_d16_hi v42, v33 offset:6256
	s_waitcnt vmcnt(2)
	ds_write_b16 v42, v26 offset:6528
	ds_write_b16_d16_hi v42, v26 offset:6800
	ds_write_b16 v42, v27 offset:7072
	ds_write_b16_d16_hi v42, v27 offset:7344
	ds_write_b16 v42, v28 offset:7616
	ds_write_b16_d16_hi v42, v28 offset:7888
	ds_write_b16 v42, v29 offset:8160
	ds_write_b16_d16_hi v42, v29 offset:8432
	s_waitcnt lgkmcnt(0)
	s_barrier
	s_and_saveexec_b64 s[8:9], vcc
	s_cbranch_execz .LBB0_449
	v_lshlrev_b32_e32 v26, 1, v1
	v_xor_b32_e32 v27, 0x7f, v26
	v_cmp_gt_u32_e32 vcc, 64, v48
	v_xor_b32_e32 v29, 0x7e, v26
	s_add_i32 s11, 0, 0x11000
	v_cndmask_b32_e32 v27, v27, v26, vcc
	v_or_b32_e32 v26, 1, v26
	v_cndmask_b32_e32 v29, v29, v26, vcc
	v_lshl_add_u32 v28, v46, 10, s11
	v_lshlrev_b32_e32 v30, 2, v27
	v_lshlrev_b32_e32 v32, 2, v29
	v_add_u32_e32 v31, v28, v30
	v_add_u32_e32 v33, v28, v32
	ds_read2st64_b32 v[26:27], v31 offset1:2
	ds_read2st64_b32 v[28:29], v33 offset1:2
	v_lshlrev_b32_e32 v34, 2, v1
	v_add_u32_e32 v35, 0xfc, v34
	v_and_b32_e32 v35, 0xfc, v35
	v_cmp_eq_u32_e32 vcc, 0, v1
	s_waitcnt lgkmcnt(0)
	v_add_f32_e32 v29, v27, v29
	v_mov_b32_e32 v34, v29
	s_nop 1
	v_add_f32_dpp v34, v34, v34 row_shr:1 row_mask:0xf bank_mask:0xf
	s_nop 1
	v_add_f32_dpp v34, v34, v34 row_shr:2 row_mask:0xf bank_mask:0xf
	s_nop 1
	v_add_f32_dpp v34, v34, v34 row_shr:4 row_mask:0xf bank_mask:0xf
	s_nop 1
	v_add_f32_dpp v34, v34, v34 row_shr:8 row_mask:0xf bank_mask:0xf
	s_nop 1
	v_add_f32_dpp v34, v34, v34 row_bcast:15 row_mask:0xa bank_mask:0xf
	s_nop 1
	v_add_f32_dpp v34, v34, v34 row_bcast:31 row_mask:0xc bank_mask:0xf
	v_sub_f32_e32 v35, v34, v29
	v_add_f32_e32 v27, v27, v35
	v_add_f32_e32 v29, v29, v35
	v_readlane_b32 s11, v34, 63
	v_sub_f32_e32 v26, v26, v27
	v_sub_f32_e32 v28, v28, v29
	v_add_f32_e32 v34, s11, v26
	v_add_f32_e32 v28, s11, v28
	v_max_f32_e32 v26, v34, v28
	ds_write_b32 v31, v27 offset:512
	ds_write_b32 v33, v29 offset:512
	v_mbcnt_lo_u32_b32 v29, -1, 0
	s_waitcnt lgkmcnt(2)
	s_nop 1
	v_max_f32_dpp v26, v26, v26 quad_perm:[1,0,3,2] row_mask:0xf bank_mask:0xf
	v_mbcnt_hi_u32_b32 v29, -1, v29
	s_waitcnt lgkmcnt(0)
	s_nop 1
	v_max_f32_dpp v26, v26, v26 quad_perm:[2,3,0,1] row_mask:0xf bank_mask:0xf
	v_lshlrev_b32_e32 v29, 2, v29
	v_xor_b32_e32 v29, 0x80, v29
	s_waitcnt lgkmcnt(0)
	s_nop 1
	v_max_f32_dpp v26, v26, v26 row_half_mirror row_mask:0xf bank_mask:0xf
	s_waitcnt lgkmcnt(0)
	s_nop 1
	v_max_f32_dpp v26, v26, v26 row_mirror row_mask:0xf bank_mask:0xf
	ds_swizzle_b32 v27, v26 offset:swizzle(SWAP,16)
	s_waitcnt lgkmcnt(0)
	v_max_f32_e32 v27, v27, v27
	v_max_f32_e32 v26, v26, v27
	ds_bpermute_b32 v27, v29, v26
	v_lshl_add_u32 v29, v46, 9, s97
	v_add_u32_e32 v30, v29, v30
	v_add_u32_e32 v29, v29, v32
	s_waitcnt lgkmcnt(0)
	v_max_f32_e32 v27, v27, v27
	v_max_f32_e32 v26, v26, v27
	v_sub_f32_e32 v27, v34, v26
	v_sub_f32_e32 v28, v28, v26
	v_mul_f32_e32 v27, 0x3fb8aa3b, v27
	v_mul_f32_e32 v28, 0x3fb8aa3b, v28
	v_exp_f32_e32 v27, v27
	v_exp_f32_e32 v28, v28
	ds_write_b32 v30, v27
	ds_write_b32 v29, v28
	s_and_b64 exec, exec, vcc
	s_cbranch_execz .LBB0_449
	v_ashrrev_i32_e32 v47, 31, v46
	v_lshlrev_b64 v[28:29], 12, v[46:47]
	v_lshl_add_u64 v[28:29], s[48:49], 0, v[28:29]
	s_ashr_i32 s55, s54, 31
	v_lshl_add_u64 v[28:29], s[54:55], 3, v[28:29]
	v_mov_b32_e32 v27, s11
	global_store_dwordx2 v[28:29], v[26:27], off

; #define LAS __attribute__((address_space(3)))
; #define SHX(v, m) (((m) < 32) ? __int_as_float(__builtin_amdgcn_ds_swizzle(__float_as_int(v), ((((m) & 31) << 10) | 0x1f))) : shx32(v))
; __device__ __forceinline__ float shfl_up_l(float v, int off, int lane) { return __int_as_float(__builtin_amdgcn_ds_bpermute(((lane - off) & 63) << 2, __float_as_int(v))); }
; __device__ __forceinline__ float shfl_l(float v, int src) { return __int_as_float(__builtin_amdgcn_ds_bpermute(src << 2, __float_as_int(v))); }
; __device__ __forceinline__ void gate_scan(const LAS float* li, LAS float* lf, int dir, int lane, int (&pos)[2], float (&b)[2], float (&x)[2], float& g) {
;     pos[0] = dir ? 127 - 2 * lane : 2 * lane; pos[1] = dir ? 126 - 2 * lane : 2 * lane + 1;
;     const float f0 = lf[pos[0]], f1 = lf[pos[1]]; const float s1 = f0 + f1; float inc = s1;
; #pragma unroll
;     for (int off = 1; off < 64; off <<= 1) { const float y = shfl_up_l(inc, off, lane); if (lane >= off) inc += y; }
;     const float exc = inc - s1; b[0] = exc + f0; b[1] = exc + s1; g = shfl_l(inc, 63);
;     lf[pos[0]] = b[0]; lf[pos[1]] = b[1];
;     x[0] = li[pos[0]] - b[0]; x[1] = li[pos[1]] - b[1];
; }
; __device__ __forceinline__ void m1_unit(LAS unsigned char* L, int u, const bf16* z, const float* gates, const float* cw, float* cloc, float* nloc, float* mg, int tid_) {
;     ...
;     if (w < 2) {
;         const int dir = w; LAS float* li = ga + dir * 256; LAS float* lf = li + 128; LAS float* wo = ga + 512 + dir * 128;
;         int pos[2]; float bq[2], xq[2], g; gate_scan(li, lf, dir, lane, pos, bq, xq, g);
;         float a0 = g + xq[0], a1 = g + xq[1], m = fmaxf(a0, a1);
;         m = fmaxf(m, SHX(m, 1)); m = fmaxf(m, SHX(m, 2)); m = fmaxf(m, SHX(m, 4)); m = fmaxf(m, SHX(m, 8)); m = fmaxf(m, SHX(m, 16)); m = fmaxf(m, SHX(m, 32));
;         wo[pos[0]] = __expf(a0 - m); wo[pos[1]] = __expf(a1 - m);
;         if (lane == 0) { mg[((size_t)dir * 512 + u) * 2 + 0] = m; mg[((size_t)dir * 512 + u) * 2 + 1] = g; }
.LBB0_463:
	s_or_b64 exec, exec, s[8:9]
	v_ashrrev_i32_e32 v42, 1, v1
	v_and_b32_e32 v49, 63, v1
	v_ashrrev_i32_e32 v46, 6, v1
	v_and_b32_e32 v42, -2, v42
	v_mul_u32_u24_e32 v43, 0x110, v45
	v_add3_u32 v42, 0, v43, v42
	v_cmp_gt_i32_e32 vcc, 2, v46
	v_lshlrev_b32_e32 v48, 2, v49
	s_waitcnt vmcnt(5)
	ds_write_b16 v42, v38
	ds_write_b16_d16_hi v42, v38 offset:272
	ds_write_b16 v42, v39 offset:544
	ds_write_b16_d16_hi v42, v39 offset:816
	ds_write_b16 v42, v40 offset:1088
	ds_write_b16_d16_hi v42, v40 offset:1360
	ds_write_b16 v42, v41 offset:1632
	ds_write_b16_d16_hi v42, v41 offset:1904
	s_waitcnt vmcnt(4)
	ds_write_b16 v42, v34 offset:2176
	ds_write_b16_d16_hi v42, v34 offset:2448
	ds_write_b16 v42, v35 offset:2720
	ds_write_b16_d16_hi v42, v35 offset:2992
	ds_write_b16 v42, v36 offset:3264
	ds_write_b16_d16_hi v42, v36 offset:3536
	ds_write_b16 v42, v37 offset:3808
	ds_write_b16_d16_hi v42, v37 offset:4080
	s_waitcnt vmcnt(3)
	ds_write_b16 v42, v30 offset:4352
	ds_write_b16_d16_hi v42, v30 offset:4624
	ds_write_b16 v42, v31 offset:4896
	ds_write_b16_d16_hi v42, v31 offset:5168
	ds_write_b16 v42, v32 offset:5440
	ds_write_b16_d16_hi v42, v32 offset:5712
	ds_write_b16 v42, v33 offset:5984
	ds_write_b16_d16_hi v42, v33 offset:6256
	s_waitcnt vmcnt(2)
	ds_write_b16 v42, v26 offset:6528
	ds_write_b16_d16_hi v42, v26 offset:6800
	ds_write_b16 v42, v27 offset:7072
	ds_write_b16_d16_hi v42, v27 offset:7344
	ds_write_b16 v42, v28 offset:7616
	ds_write_b16_d16_hi v42, v28 offset:7888
	ds_write_b16 v42, v29 offset:8160
	ds_write_b16_d16_hi v42, v29 offset:8432
	s_waitcnt lgkmcnt(0)
	s_barrier
	s_and_saveexec_b64 s[8:9], vcc
	s_cbranch_execz .LBB0_466
	v_lshlrev_b32_e32 v26, 1, v49
	v_xor_b32_e32 v27, 0x7f, v26
	v_cmp_gt_u32_e32 vcc, 64, v1
	v_xor_b32_e32 v29, 0x7e, v26
	s_add_i32 s4, 0, 0x11000
	v_cndmask_b32_e32 v27, v27, v26, vcc
	v_or_b32_e32 v26, 1, v26
	v_cndmask_b32_e32 v29, v29, v26, vcc
	v_lshl_add_u32 v28, v46, 10, s4
	v_lshlrev_b32_e32 v30, 2, v27
	v_lshlrev_b32_e32 v32, 2, v29
	v_add_u32_e32 v31, v28, v30
	v_add_u32_e32 v33, v28, v32
	ds_read2st64_b32 v[26:27], v31 offset1:2
	ds_read2st64_b32 v[28:29], v33 offset1:2
	v_add_u32_e32 v34, 0xfc, v48
	v_and_b32_e32 v34, 0xfc, v34
	v_cmp_eq_u32_e32 vcc, 0, v49
	v_add_u32_e32 v35, 0xf8, v48
	s_waitcnt lgkmcnt(0)
	v_add_f32_e32 v29, v27, v29
	v_mov_b32_e32 v34, v29
	s_nop 1
	v_add_f32_dpp v34, v34, v34 row_shr:1 row_mask:0xf bank_mask:0xf
	s_nop 1
	v_add_f32_dpp v34, v34, v34 row_shr:2 row_mask:0xf bank_mask:0xf
	s_nop 1
	v_add_f32_dpp v34, v34, v34 row_shr:4 row_mask:0xf bank_mask:0xf
	s_nop 1
	v_add_f32_dpp v34, v34, v34 row_shr:8 row_mask:0xf bank_mask:0xf
	s_nop 1
	v_add_f32_dpp v34, v34, v34 row_bcast:15 row_mask:0xa bank_mask:0xf
	s_nop 1
	v_add_f32_dpp v34, v34, v34 row_bcast:31 row_mask:0xc bank_mask:0xf
	v_sub_f32_e32 v35, v34, v29
	v_add_f32_e32 v27, v27, v35
	v_add_f32_e32 v29, v29, v35
	v_readlane_b32 s4, v34, 63
	v_sub_f32_e32 v26, v26, v27
	v_sub_f32_e32 v28, v28, v29
	v_add_f32_e32 v34, s4, v26
	v_add_f32_e32 v28, s4, v28
	v_max_f32_e32 v26, v34, v28
	ds_write_b32 v31, v27 offset:512
	ds_write_b32 v33, v29 offset:512
	v_mbcnt_lo_u32_b32 v29, -1, 0
	s_waitcnt lgkmcnt(2)
	s_nop 1
	v_max_f32_dpp v26, v26, v26 quad_perm:[1,0,3,2] row_mask:0xf bank_mask:0xf
	v_mbcnt_hi_u32_b32 v29, -1, v29
	s_waitcnt lgkmcnt(0)
	s_nop 1
	v_max_f32_dpp v26, v26, v26 quad_perm:[2,3,0,1] row_mask:0xf bank_mask:0xf
	v_lshlrev_b32_e32 v29, 2, v29
	v_xor_b32_e32 v29, 0x80, v29
	s_waitcnt lgkmcnt(0)
	s_nop 1
	v_max_f32_dpp v26, v26, v26 row_half_mirror row_mask:0xf bank_mask:0xf
	s_waitcnt lgkmcnt(0)
	s_nop 1
	v_max_f32_dpp v26, v26, v26 row_mirror row_mask:0xf bank_mask:0xf
	ds_swizzle_b32 v27, v26 offset:swizzle(SWAP,16)
	s_waitcnt lgkmcnt(0)
	v_max_f32_e32 v27, v27, v27
	v_max_f32_e32 v26, v26, v27
	ds_bpermute_b32 v27, v29, v26
	v_lshl_add_u32 v29, v46, 9, s97
	v_add_u32_e32 v30, v29, v30
	v_add_u32_e32 v29, v29, v32
	s_waitcnt lgkmcnt(0)
	v_max_f32_e32 v27, v27, v27
	v_max_f32_e32 v26, v26, v27
	v_sub_f32_e32 v27, v34, v26
	v_sub_f32_e32 v28, v28, v26
	v_mul_f32_e32 v27, 0x3fb8aa3b, v27
	v_mul_f32_e32 v28, 0x3fb8aa3b, v28
	v_exp_f32_e32 v27, v27
	v_exp_f32_e32 v28, v28
	ds_write_b32 v30, v27
	ds_write_b32 v29, v28
	s_and_b64 exec, exec, vcc
	s_cbranch_execz .LBB0_466
	v_ashrrev_i32_e32 v47, 31, v46
	v_lshlrev_b64 v[28:29], 12, v[46:47]
	v_lshl_add_u64 v[28:29], s[46:47], 0, v[28:29]
	v_lshl_add_u64 v[28:29], s[16:17], 3, v[28:29]
	v_mov_b32_e32 v27, s4
	global_store_dwordx2 v[28:29], v[26:27], off

; __device__ __forceinline__ unsigned pk2(float lo, float hi) { unsigned r; asm("v_cvt_pk_bf16_f32 %0, %1, %2" : "=v"(r) : "v"(lo), "v"(hi)); return r; }
; __device__ __forceinline__ float bflo(unsigned w) { return __uint_as_float(w << 16); }
; __device__ __forceinline__ float bfhi(unsigned w) { return __uint_as_float(w & 0xffff0000u); }
; __device__ __forceinline__ float siluf_(float x) { return x * __builtin_amdgcn_rcpf(1.f + __expf(-x)); }
; __device__ __forceinline__ void conv_compute(const ZR6& r, const float* cw, int wcol, float (&o)[16]) {
;     const unsigned pw[8] = {r.p0.x, r.p0.y, r.p0.z, r.p0.w, r.p1.x, r.p1.y, r.p1.z, r.p1.w}, cwd[8] = {r.c0.x, r.c0.y, r.c0.z, r.c0.w, r.c1.x, r.c1.y, r.c1.z, r.c1.w}, nw[8] = {r.n0.x, r.n0.y, r.n0.z, r.n0.w, r.n1.x, r.n1.y, r.n1.z, r.n1.w};
;     float w0[16], w1[16], w2[16];
; #pragma unroll
;     for (int q = 0; q < 4; ++q) { const f32x4 a0 = *(const f32x4*)(cw + wcol + 4 * q), a1 = *(const f32x4*)(cw + 512 + wcol + 4 * q), a2 = *(const f32x4*)(cw + 1024 + wcol + 4 * q);
; #pragma unroll
;         for (int j = 0; j < 4; ++j) { w0[4 * q + j] = a0[j]; w1[4 * q + j] = a1[j]; w2[4 * q + j] = a2[j]; } }
; #pragma unroll
;     for (int i = 0; i < 8; ++i) {
;         o[2 * i] = siluf_(w0[2 * i] * bflo(pw[i]) + w1[2 * i] * bflo(cwd[i]) + w2[2 * i] * bflo(nw[i]));
;         o[2 * i + 1] = siluf_(w0[2 * i + 1] * bfhi(pw[i]) + w1[2 * i + 1] * bfhi(cwd[i]) + w2[2 * i + 1] * bfhi(nw[i])); }
; }
; __device__ __forceinline__ void m3_unit(LAS unsigned char* L, int u, const bf16* z, const float* gates, const float* cw, const bf16* cprev, const float* nprev, const float* mprev, const float* normg, bf16* mix, int tid_) {
;     ...
;     { const int s = tid >> 2, part = tid & 3; float o[16];
;       conv_compute(zq, cw, hh * 64 + part * 16, o);
;       v4u w0, w1; w0.x = pk2(o[0] * 0.125f, o[1] * 0.125f); w0.y = pk2(o[2] * 0.125f, o[3] * 0.125f); w0.z = pk2(o[4] * 0.125f, o[5] * 0.125f); w0.w = pk2(o[6] * 0.125f, o[7] * 0.125f);
.LBB0_798:
	s_or_b64 exec, exec, s[8:9]
	v_lshlrev_b32_e32 v102, 2, v66
	global_load_dwordx4 v[66:69], v102, s[92:93] offset:48
	global_load_dwordx4 v[78:81], v102, s[92:93] offset:32
	global_load_dwordx4 v[90:93], v102, s[92:93] offset:16
	global_load_dwordx4 v[106:109], v102, s[92:93]
	global_load_dwordx4 v[70:73], v102, s[92:93] offset:2096
	global_load_dwordx4 v[82:85], v102, s[92:93] offset:2080
	global_load_dwordx4 v[94:97], v102, s[92:93] offset:2064
	global_load_dwordx4 v[112:115], v102, s[92:93] offset:2048
	global_load_dwordx4 v[74:77], v102, s[6:7] offset:48
	global_load_dwordx4 v[86:89], v102, s[6:7] offset:32
	global_load_dwordx4 v[98:101], v102, s[6:7] offset:16
	global_load_dwordx4 v[120:123], v102, s[6:7]
	s_waitcnt vmcnt(19)
	v_lshlrev_b32_e32 v117, 16, v62
	v_lshlrev_b32_e32 v116, 16, v58
	s_waitcnt vmcnt(18)
	v_lshlrev_b32_e32 v105, 16, v54
	v_and_b32_e32 v54, 0xffff0000, v54
	v_and_b32_e32 v162, 15, v110
	v_mul_u32_u24_e32 v1, 0x110, v1
	v_and_b32_e32 v158, 48, v110
	v_mov_b32_e32 v159, v163
	s_movk_i32 s4, 0x1000
	v_ashrrev_i32_e32 v111, 6, v110
	v_and_b32_e32 v119, 63, v110
	s_waitcnt vmcnt(8)
	v_mov_b32_e32 v124, v106
	s_waitcnt vmcnt(0)
	v_mov_b32_e32 v125, v120
	v_pk_mul_f32 v[116:117], v[124:125], v[116:117]
	v_mov_b32_e32 v120, v107
	v_fma_f32 v105, v112, v105, v116
	v_add_f32_e32 v105, v105, v117
	v_mul_f32_e32 v106, 0xbfb8aa3b, v105
	v_exp_f32_e32 v106, v106
	v_and_b32_e32 v117, 0xffff0000, v62
	v_and_b32_e32 v116, 0xffff0000, v58
	v_mov_b32_e32 v112, v108
	v_add_f32_e32 v106, 1.0, v106
	v_rcp_f32_e32 v106, v106
	s_nop 0
	v_mul_f32_e32 v105, v105, v106
	v_pk_mul_f32 v[106:107], v[120:121], v[116:117]
	s_nop 0
	v_fma_f32 v54, v113, v54, v106
	v_add_f32_e32 v54, v54, v107
	v_mul_f32_e32 v58, 0xbfb8aa3b, v54
	v_exp_f32_e32 v58, v58
	v_lshlrev_b32_e32 v106, 16, v59
	v_lshlrev_b32_e32 v107, 16, v63
	v_mov_b32_e32 v113, v122
	v_add_f32_e32 v58, 1.0, v58
	v_rcp_f32_e32 v58, v58
	v_pk_mul_f32 v[106:107], v[112:113], v[106:107]
	v_and_b32_e32 v63, 0xffff0000, v63
	v_mov_b32_e32 v122, v109
	v_mul_f32_e32 v54, v54, v58
	v_lshlrev_b32_e32 v58, 16, v55
	v_fma_f32 v58, v114, v58, v106
	v_add_f32_e32 v58, v58, v107
	v_mul_f32_e32 v62, 0xbfb8aa3b, v58
	v_exp_f32_e32 v62, v62
	v_and_b32_e32 v55, 0xffff0000, v55
	v_mov_b32_e32 v106, v90
	v_mov_b32_e32 v107, v98
	v_add_f32_e32 v62, 1.0, v62
	v_rcp_f32_e32 v62, v62
	v_mov_b32_e32 v98, v91
	v_mov_b32_e32 v90, v92
	v_mov_b32_e32 v91, v100
	v_mul_f32_e32 v58, v58, v62
	v_and_b32_e32 v62, 0xffff0000, v59
	v_pk_mul_f32 v[62:63], v[122:123], v[62:63]
	v_mov_b32_e32 v100, v93
	v_fma_f32 v55, v115, v55, v62
	v_add_f32_e32 v55, v55, v63
	v_mul_f32_e32 v59, 0xbfb8aa3b, v55
	v_exp_f32_e32 v59, v59
	v_lshlrev_b32_e32 v63, 16, v64
	v_lshlrev_b32_e32 v62, 16, v60
	v_pk_mul_f32 v[62:63], v[106:107], v[62:63]
	v_add_f32_e32 v59, 1.0, v59
	v_rcp_f32_e32 v59, v59
	v_lshlrev_b32_e32 v93, 16, v38
	v_lshlrev_b32_e32 v92, 16, v34
	v_mul_f32_e32 v55, v55, v59
	v_lshlrev_b32_e32 v59, 16, v56
	v_fma_f32 v59, v94, v59, v62
	v_add_f32_e32 v59, v59, v63
	v_mul_f32_e32 v62, 0xbfb8aa3b, v59
	v_exp_f32_e32 v62, v62
	v_and_b32_e32 v63, 0xffff0000, v64
	v_and_b32_e32 v56, 0xffff0000, v56
	v_add_f32_e32 v62, 1.0, v62
	v_rcp_f32_e32 v62, v62
	s_nop 0
	v_mul_f32_e32 v59, v59, v62
	v_and_b32_e32 v62, 0xffff0000, v60
	v_pk_mul_f32 v[62:63], v[98:99], v[62:63]
	s_nop 0
	v_fma_f32 v56, v95, v56, v62
	v_add_f32_e32 v56, v56, v63
	v_mul_f32_e32 v60, 0xbfb8aa3b, v56
	v_exp_f32_e32 v60, v60
	v_lshlrev_b32_e32 v62, 16, v61
	v_lshlrev_b32_e32 v63, 16, v65
	v_pk_mul_f32 v[62:63], v[90:91], v[62:63]
	v_add_f32_e32 v60, 1.0, v60
	v_rcp_f32_e32 v60, v60
	v_lshlrev_b32_e32 v91, 16, v30
	v_and_b32_e32 v30, 0xffff0000, v30
	v_mul_f32_e32 v56, v56, v60
	v_lshlrev_b32_e32 v60, 16, v57
	v_fma_f32 v60, v96, v60, v62
	v_add_f32_e32 v60, v60, v63
	v_mul_f32_e32 v62, 0xbfb8aa3b, v60
	v_exp_f32_e32 v62, v62
	v_and_b32_e32 v63, 0xffff0000, v65
	v_and_b32_e32 v57, 0xffff0000, v57
	v_lshlrev_b32_e32 v65, 16, v42
	v_add_f32_e32 v62, 1.0, v62
	v_rcp_f32_e32 v62, v62
	v_and_b32_e32 v42, 0xffff0000, v42
	v_mul_f32_e32 v64, v60, v62
	v_and_b32_e32 v62, 0xffff0000, v61
	v_pk_mul_f32 v[60:61], v[100:101], v[62:63]
	v_mov_b32_e32 v62, v78
	v_fma_f32 v57, v97, v57, v60
	v_add_f32_e32 v57, v57, v61
	v_mul_f32_e32 v60, 0xbfb8aa3b, v57
	v_exp_f32_e32 v60, v60
	v_lshlrev_b32_e32 v61, 16, v50
	v_mov_b32_e32 v63, v86
	v_mov_b32_e32 v86, v79
	v_add_f32_e32 v60, 1.0, v60
	v_rcp_f32_e32 v60, v60
	s_nop 0
	v_mul_f32_e32 v57, v57, v60
	v_lshlrev_b32_e32 v60, 16, v46
	v_pk_mul_f32 v[60:61], v[62:63], v[60:61]
	v_mov_b32_e32 v62, v80
	v_fma_f32 v60, v82, v65, v60
	v_add_f32_e32 v60, v60, v61
	v_mul_f32_e32 v61, 0xbfb8aa3b, v60
	v_exp_f32_e32 v61, v61
	v_mov_b32_e32 v63, v88
	v_mov_b32_e32 v88, v81
	v_add_f32_e32 v61, 1.0, v61
	v_rcp_f32_e32 v61, v61
	s_nop 0
	v_mul_f32_e32 v65, v60, v61
	v_and_b32_e32 v61, 0xffff0000, v50
	v_and_b32_e32 v60, 0xffff0000, v46
	v_pk_mul_f32 v[60:61], v[86:87], v[60:61]
	v_or_b32_e32 v86, 0x400, v102
	v_fma_f32 v42, v83, v42, v60
	v_add_f32_e32 v42, v42, v61
	v_mul_f32_e32 v46, 0xbfb8aa3b, v42
	v_exp_f32_e32 v46, v46
	v_lshlrev_b32_e32 v60, 16, v47
	v_lshlrev_b32_e32 v61, 16, v51
	v_pk_mul_f32 v[60:61], v[62:63], v[60:61]
	v_add_f32_e32 v46, 1.0, v46
	v_rcp_f32_e32 v46, v46
	s_nop 0
	v_mul_f32_e32 v50, v42, v46
	v_lshlrev_b32_e32 v42, 16, v43
	v_fma_f32 v42, v84, v42, v60
	v_add_f32_e32 v42, v42, v61
	v_mul_f32_e32 v46, 0xbfb8aa3b, v42
	v_exp_f32_e32 v46, v46
	v_lshlrev_b32_e32 v61, 16, v44
	v_and_b32_e32 v44, 0xffff0000, v44
	v_add_f32_e32 v46, 1.0, v46
	v_rcp_f32_e32 v46, v46
	s_nop 0
	v_mul_f32_e32 v60, v42, v46
; #define LAS __attribute__((address_space(3)))
; __device__ __forceinline__ unsigned pk2(float lo, float hi) { unsigned r; asm("v_cvt_pk_bf16_f32 %0, %1, %2" : "=v"(r) : "v"(lo), "v"(hi)); return r; }
; __device__ __forceinline__ void m3_unit(LAS unsigned char* L, int u, const bf16* z, const float* gates, const float* cw, const bf16* cprev, const float* nprev, const float* mprev, const float* normg, bf16* mix, int tid_) {
;     ...
;       conv_compute(zq, cw, hh * 64 + part * 16, o);
;       v4u w0, w1; w0.x = pk2(o[0] * 0.125f, o[1] * 0.125f); w0.y = pk2(o[2] * 0.125f, o[3] * 0.125f); w0.z = pk2(o[4] * 0.125f, o[5] * 0.125f); w0.w = pk2(o[6] * 0.125f, o[7] * 0.125f);
;       w1.x = pk2(o[8] * 0.125f, o[9] * 0.125f); w1.y = pk2(o[10] * 0.125f, o[11] * 0.125f); w1.z = pk2(o[12] * 0.125f, o[13] * 0.125f); w1.w = pk2(o[14] * 0.125f, o[15] * 0.125f);
;       *(LAS v4u*)(L + QS + s * 144 + part * 32) = w0; *(LAS v4u*)(L + QS + s * 144 + part * 32 + 16) = w1;
;       conv_compute(zk, cw, 256 + hh * 64 + part * 16, o);
;       w0.x = pk2(o[0], o[1]); w0.y = pk2(o[2], o[3]); w0.z = pk2(o[4], o[5]); w0.w = pk2(o[6], o[7]); w1.x = pk2(o[8], o[9]); w1.y = pk2(o[10], o[11]); w1.z = pk2(o[12], o[13]); w1.w = pk2(o[14], o[15]);
;       *(LAS v4u*)(L + KS + s * 144 + part * 32) = w0; *(LAS v4u*)(L + KS + s * 144 + part * 32 + 16) = w1; }
	v_and_b32_e32 v46, 0xffff0000, v43
	v_and_b32_e32 v43, 0xffff0000, v51
	v_and_b32_e32 v42, 0xffff0000, v47
	v_pk_mul_f32 v[42:43], v[88:89], v[42:43]
	v_mov_b32_e32 v47, v74
	v_fma_f32 v42, v85, v46, v42
	v_add_f32_e32 v42, v42, v43
	v_mul_f32_e32 v43, 0xbfb8aa3b, v42
	v_exp_f32_e32 v43, v43
	v_mov_b32_e32 v46, v66
	v_mov_b32_e32 v74, v67
	v_add_f32_e32 v43, 1.0, v43
	v_rcp_f32_e32 v43, v43
	s_nop 0
	v_mul_f32_e32 v51, v42, v43
	v_lshlrev_b32_e32 v43, 16, v52
	v_lshlrev_b32_e32 v42, 16, v48
	v_pk_mul_f32 v[42:43], v[46:47], v[42:43]
	v_mov_b32_e32 v46, v68
	v_fma_f32 v42, v70, v61, v42
	v_add_f32_e32 v42, v42, v43
	v_mul_f32_e32 v43, 0xbfb8aa3b, v42
	v_exp_f32_e32 v43, v43
	v_mov_b32_e32 v47, v76
	v_mov_b32_e32 v76, v69
	v_add_f32_e32 v43, 1.0, v43
	v_rcp_f32_e32 v43, v43
	s_nop 0
	v_mul_f32_e32 v61, v42, v43
	v_and_b32_e32 v43, 0xffff0000, v52
	v_and_b32_e32 v42, 0xffff0000, v48
	v_pk_mul_f32 v[42:43], v[74:75], v[42:43]
	s_nop 0
	v_fma_f32 v42, v71, v44, v42
	v_add_f32_e32 v42, v42, v43
	v_mul_f32_e32 v43, 0xbfb8aa3b, v42
	v_exp_f32_e32 v43, v43
	v_lshlrev_b32_e32 v44, 16, v45
	v_add_f32_e32 v43, 1.0, v43
	v_rcp_f32_e32 v43, v43
	s_nop 0
	v_mul_f32_e32 v48, v42, v43
	v_lshlrev_b32_e32 v42, 16, v49
	v_lshlrev_b32_e32 v43, 16, v53
	v_pk_mul_f32 v[42:43], v[46:47], v[42:43]
	v_mul_f32_e32 v46, 0x3e000000, v57
	v_fma_f32 v42, v72, v44, v42
	v_add_f32_e32 v42, v42, v43
	v_mul_f32_e32 v43, 0xbfb8aa3b, v42
	v_exp_f32_e32 v43, v43
	v_and_b32_e32 v44, 0xffff0000, v45
	v_mul_f32_e32 v45, 0x3e000000, v56
	v_mul_f32_e32 v47, 0x3e000000, v50
	v_add_f32_e32 v43, 1.0, v43
	v_rcp_f32_e32 v43, v43
	v_mul_f32_e32 v50, 0x3e000000, v51
	v_mul_f32_e32 v48, 0x3e000000, v48
	v_lshlrev_b32_e32 v51, 5, v104
	v_mul_f32_e32 v52, v42, v43
	v_and_b32_e32 v43, 0xffff0000, v53
	v_and_b32_e32 v42, 0xffff0000, v49
	v_pk_mul_f32 v[42:43], v[76:77], v[42:43]
	s_nop 0
	v_fma_f32 v42, v73, v44, v42
	v_add_f32_e32 v42, v42, v43
	v_mul_f32_e32 v43, 0xbfb8aa3b, v42
	v_exp_f32_e32 v43, v43
	v_mul_f32_e32 v44, 0x3e000000, v55
	v_add_f32_e32 v43, 1.0, v43
	v_rcp_f32_e32 v43, v43
	s_nop 0
	v_mul_f32_e32 v49, v42, v43
	v_mul_f32_e32 v42, 0x3e000000, v105
	v_mul_f32_e32 v43, 0x3e000000, v54
	v_cvt_pk_bf16_f32 v42, v42, v43
	v_mul_f32_e32 v43, 0x3e000000, v58
	v_cvt_pk_bf16_f32 v43, v43, v44
	v_mul_f32_e32 v44, 0x3e000000, v59
	v_cvt_pk_bf16_f32 v44, v44, v45
	v_mul_f32_e32 v45, 0x3e000000, v64
	v_cvt_pk_bf16_f32 v45, v45, v46
	v_mul_f32_e32 v46, 0x3e000000, v65
	v_cvt_pk_bf16_f32 v46, v46, v47
	v_mul_f32_e32 v47, 0x3e000000, v60
	v_cvt_pk_bf16_f32 v47, v47, v50
	v_mul_f32_e32 v50, 0x3e000000, v61
	v_cvt_pk_bf16_f32 v48, v50, v48
	v_mul_f32_e32 v50, 0x3e000000, v52
	v_mul_f32_e32 v49, 0x3e000000, v49
	v_cvt_pk_bf16_f32 v49, v50, v49
	v_mul_lo_u32 v50, v103, s84
	v_add3_u32 v90, 0, v50, v51
	ds_write_b128 v90, v[42:45]
	ds_write_b128 v90, v[46:49] offset:16
	global_load_dwordx4 v[42:45], v102, s[92:93] offset:1072
	global_load_dwordx4 v[54:57], v102, s[92:93] offset:1056
	global_load_dwordx4 v[66:69], v102, s[92:93] offset:1040
	global_load_dwordx4 v[78:81], v102, s[92:93] offset:1024
	global_load_dwordx4 v[46:49], v102, s[92:93] offset:3120
	global_load_dwordx4 v[58:61], v102, s[92:93] offset:3104
	global_load_dwordx4 v[70:73], v102, s[92:93] offset:3088
	global_load_dwordx4 v[82:85], v102, s[92:93] offset:3072
	global_load_dwordx4 v[50:53], v86, s[6:7] offset:48
	global_load_dwordx4 v[62:65], v86, s[6:7] offset:32
	global_load_dwordx4 v[74:77], v86, s[6:7] offset:16
	s_nop 0
	global_load_dwordx4 v[86:89], v86, s[6:7]
	s_waitcnt vmcnt(8)
	v_mov_b32_e32 v94, v78
	s_waitcnt vmcnt(0)
	v_mov_b32_e32 v95, v86
	v_pk_mul_f32 v[92:93], v[94:95], v[92:93]
	v_mov_b32_e32 v86, v79
	v_fma_f32 v78, v82, v91, v92
	v_add_f32_e32 v78, v78, v93
	v_mul_f32_e32 v82, 0xbfb8aa3b, v78
	v_exp_f32_e32 v82, v82
	v_and_b32_e32 v93, 0xffff0000, v38
	v_and_b32_e32 v92, 0xffff0000, v34
	v_add_f32_e32 v82, 1.0, v82
	v_rcp_f32_e32 v82, v82
	s_nop 0
	v_mul_f32_e32 v91, v78, v82
	v_pk_mul_f32 v[78:79], v[86:87], v[92:93]
	v_mov_b32_e32 v82, v80
	v_fma_f32 v30, v83, v30, v78
	v_add_f32_e32 v30, v30, v79
	v_mul_f32_e32 v34, 0xbfb8aa3b, v30
	v_exp_f32_e32 v34, v34
	v_lshlrev_b32_e32 v78, 16, v35
	v_lshlrev_b32_e32 v79, 16, v39
	v_mov_b32_e32 v83, v88
	v_add_f32_e32 v34, 1.0, v34
	v_rcp_f32_e32 v34, v34
	v_pk_mul_f32 v[78:79], v[82:83], v[78:79]
	v_mov_b32_e32 v88, v81
	v_mul_f32_e32 v38, v30, v34
	v_lshlrev_b32_e32 v30, 16, v31
	v_fma_f32 v30, v84, v30, v78
	v_add_f32_e32 v30, v30, v79
	v_mul_f32_e32 v34, 0xbfb8aa3b, v30
	v_exp_f32_e32 v34, v34
	v_lshlrev_b32_e32 v79, 16, v32
	v_and_b32_e32 v32, 0xffff0000, v32
	v_add_f32_e32 v34, 1.0, v34
	v_rcp_f32_e32 v34, v34
	s_nop 0
	v_mul_f32_e32 v78, v30, v34
	v_and_b32_e32 v34, 0xffff0000, v31
	v_and_b32_e32 v31, 0xffff0000, v39
	v_and_b32_e32 v30, 0xffff0000, v35
	v_pk_mul_f32 v[30:31], v[88:89], v[30:31]
	v_mov_b32_e32 v35, v74
	v_fma_f32 v30, v85, v34, v30
	v_add_f32_e32 v30, v30, v31
	v_mul_f32_e32 v31, 0xbfb8aa3b, v30
	v_exp_f32_e32 v31, v31
	v_mov_b32_e32 v34, v66
	v_mov_b32_e32 v74, v67
	v_add_f32_e32 v31, 1.0, v31
	v_rcp_f32_e32 v31, v31
	s_nop 0
	v_mul_f32_e32 v39, v30, v31
	v_lshlrev_b32_e32 v31, 16, v40
	v_lshlrev_b32_e32 v30, 16, v36
	v_pk_mul_f32 v[30:31], v[34:35], v[30:31]
	v_mov_b32_e32 v34, v68
	v_fma_f32 v30, v70, v79, v30
	v_add_f32_e32 v30, v30, v31
	v_mul_f32_e32 v31, 0xbfb8aa3b, v30
	v_exp_f32_e32 v31, v31
	v_mov_b32_e32 v35, v76
	v_mov_b32_e32 v76, v69
	v_add_f32_e32 v31, 1.0, v31
	v_rcp_f32_e32 v31, v31
	s_nop 0
	v_mul_f32_e32 v66, v30, v31
	v_and_b32_e32 v31, 0xffff0000, v40
	v_and_b32_e32 v30, 0xffff0000, v36
	v_pk_mul_f32 v[30:31], v[74:75], v[30:31]
; #define LAS __attribute__((address_space(3)))
; __device__ __forceinline__ unsigned pk2(float lo, float hi) { unsigned r; asm("v_cvt_pk_bf16_f32 %0, %1, %2" : "=v"(r) : "v"(lo), "v"(hi)); return r; }
; __device__ __forceinline__ void vT_store(LAS unsigned char* VT, const VR4& r, int tid) { const int s = tid >> 2, part = tid & 3;
; #pragma unroll
;     for (int q = 0; q < 4; ++q) { const unsigned ww[4] = {r.q[q].x, r.q[q].y, r.q[q].z, r.q[q].w};
; #pragma unroll
;         for (int i = 0; i < 4; ++i) { const int e = part * 32 + q * 8 + 2 * i; *(LAS bf16*)(VT + e * 272 + s * 2) = (bf16)(ww[i] & 0xffffu); *(LAS bf16*)(VT + (e + 1) * 272 + s * 2) = (bf16)(ww[i] >> 16); } } }
; __device__ __forceinline__ void m3_unit(LAS unsigned char* L, int u, const bf16* z, const float* gates, const float* cw, const bf16* cprev, const float* nprev, const float* mprev, const float* normg, bf16* mix, int tid_) {
;     ...
;       conv_compute(zk, cw, 256 + hh * 64 + part * 16, o);
;       w0.x = pk2(o[0], o[1]); w0.y = pk2(o[2], o[3]); w0.z = pk2(o[4], o[5]); w0.w = pk2(o[6], o[7]); w1.x = pk2(o[8], o[9]); w1.y = pk2(o[10], o[11]); w1.z = pk2(o[12], o[13]); w1.w = pk2(o[14], o[15]);
;       *(LAS v4u*)(L + KS + s * 144 + part * 32) = w0; *(LAS v4u*)(L + KS + s * 144 + part * 32 + 16) = w1; }
;     vT_store(L + VT, vr, tid);
	s_nop 0
	v_fma_f32 v30, v71, v32, v30
	v_add_f32_e32 v30, v30, v31
	v_mul_f32_e32 v31, 0xbfb8aa3b, v30
	v_exp_f32_e32 v31, v31
	v_lshlrev_b32_e32 v32, 16, v33
	v_add_f32_e32 v31, 1.0, v31
	v_rcp_f32_e32 v31, v31
	s_nop 0
	v_mul_f32_e32 v36, v30, v31
	v_lshlrev_b32_e32 v30, 16, v37
	v_lshlrev_b32_e32 v31, 16, v41
	v_pk_mul_f32 v[30:31], v[34:35], v[30:31]
	s_nop 0
	v_fma_f32 v30, v72, v32, v30
	v_add_f32_e32 v30, v30, v31
	v_mul_f32_e32 v31, 0xbfb8aa3b, v30
	v_exp_f32_e32 v31, v31
	v_and_b32_e32 v32, 0xffff0000, v33
	v_mov_b32_e32 v33, v62
	v_mov_b32_e32 v62, v55
	v_add_f32_e32 v31, 1.0, v31
	v_rcp_f32_e32 v31, v31
	s_nop 0
	v_mul_f32_e32 v34, v30, v31
	v_and_b32_e32 v31, 0xffff0000, v41
	v_and_b32_e32 v30, 0xffff0000, v37
	v_pk_mul_f32 v[30:31], v[76:77], v[30:31]
	v_lshlrev_b32_e32 v37, 16, v2
	v_fma_f32 v30, v73, v32, v30
	v_add_f32_e32 v30, v30, v31
	v_mul_f32_e32 v31, 0xbfb8aa3b, v30
	v_exp_f32_e32 v31, v31
	v_mov_b32_e32 v32, v54
	v_and_b32_e32 v2, 0xffff0000, v2
	v_add_f32_e32 v31, 1.0, v31
	v_rcp_f32_e32 v31, v31
	s_nop 0
	v_mul_f32_e32 v35, v30, v31
	v_lshlrev_b32_e32 v31, 16, v18
	v_lshlrev_b32_e32 v30, 16, v6
	v_pk_mul_f32 v[30:31], v[32:33], v[30:31]
	v_mov_b32_e32 v32, v56
	v_fma_f32 v30, v58, v37, v30
	v_add_f32_e32 v30, v30, v31
	v_mul_f32_e32 v31, 0xbfb8aa3b, v30
	v_exp_f32_e32 v31, v31
	v_mov_b32_e32 v33, v64
	v_mov_b32_e32 v64, v57
	v_add_f32_e32 v31, 1.0, v31
	v_rcp_f32_e32 v31, v31
	s_nop 0
	v_mul_f32_e32 v37, v30, v31
	v_and_b32_e32 v31, 0xffff0000, v18
	v_and_b32_e32 v30, 0xffff0000, v6
	v_pk_mul_f32 v[30:31], v[62:63], v[30:31]
	s_nop 0
	v_fma_f32 v2, v59, v2, v30
	v_add_f32_e32 v2, v2, v31
	v_mul_f32_e32 v6, 0xbfb8aa3b, v2
	v_exp_f32_e32 v6, v6
	v_lshlrev_b32_e32 v30, 16, v7
	v_lshlrev_b32_e32 v31, 16, v19
	v_pk_mul_f32 v[30:31], v[32:33], v[30:31]
	v_add_f32_e32 v6, 1.0, v6
	v_rcp_f32_e32 v6, v6
	s_nop 0
	v_mul_f32_e32 v18, v2, v6
	v_lshlrev_b32_e32 v2, 16, v3
	v_fma_f32 v2, v60, v2, v30
	v_add_f32_e32 v2, v2, v31
	v_mul_f32_e32 v6, 0xbfb8aa3b, v2
	v_exp_f32_e32 v6, v6
	v_lshlrev_b32_e32 v31, 16, v4
	v_and_b32_e32 v4, 0xffff0000, v4
	v_add_f32_e32 v6, 1.0, v6
	v_rcp_f32_e32 v6, v6
	s_nop 0
	v_mul_f32_e32 v30, v2, v6
	v_and_b32_e32 v6, 0xffff0000, v3
	v_and_b32_e32 v3, 0xffff0000, v19
	v_and_b32_e32 v2, 0xffff0000, v7
	v_pk_mul_f32 v[2:3], v[64:65], v[2:3]
	v_mov_b32_e32 v7, v50
	v_fma_f32 v2, v61, v6, v2
	v_add_f32_e32 v2, v2, v3
	v_mul_f32_e32 v3, 0xbfb8aa3b, v2
	v_exp_f32_e32 v3, v3
	v_mov_b32_e32 v6, v42
	v_mov_b32_e32 v50, v43
	v_add_f32_e32 v3, 1.0, v3
	v_rcp_f32_e32 v3, v3
	s_nop 0
	v_mul_f32_e32 v19, v2, v3
	v_lshlrev_b32_e32 v3, 16, v20
	v_lshlrev_b32_e32 v2, 16, v8
	v_pk_mul_f32 v[2:3], v[6:7], v[2:3]
	v_mov_b32_e32 v6, v44
	v_fma_f32 v2, v46, v31, v2
	v_add_f32_e32 v2, v2, v3
	v_mul_f32_e32 v3, 0xbfb8aa3b, v2
	v_exp_f32_e32 v3, v3
	v_mov_b32_e32 v7, v52
	v_mov_b32_e32 v52, v45
	v_add_f32_e32 v3, 1.0, v3
	v_rcp_f32_e32 v3, v3
	s_nop 0
	v_mul_f32_e32 v31, v2, v3
	v_and_b32_e32 v3, 0xffff0000, v20
	v_and_b32_e32 v2, 0xffff0000, v8
	v_pk_mul_f32 v[2:3], v[50:51], v[2:3]
	s_nop 0
	v_fma_f32 v2, v47, v4, v2
	v_add_f32_e32 v2, v2, v3
	v_mul_f32_e32 v3, 0xbfb8aa3b, v2
	v_exp_f32_e32 v3, v3
	v_lshlrev_b32_e32 v4, 16, v5
	v_add_f32_e32 v3, 1.0, v3
	v_rcp_f32_e32 v3, v3
	s_nop 0
	v_mul_f32_e32 v8, v2, v3
	v_lshlrev_b32_e32 v2, 16, v9
	v_lshlrev_b32_e32 v3, 16, v21
	v_pk_mul_f32 v[2:3], v[6:7], v[2:3]
	v_cvt_pk_bf16_f32 v6, v37, v18
	v_cvt_pk_bf16_f32 v7, v30, v19
	v_cvt_pk_bf16_f32 v8, v31, v8
	s_nop 0
	v_fma_f32 v2, v48, v4, v2
	v_add_f32_e32 v2, v2, v3
	v_mul_f32_e32 v3, 0xbfb8aa3b, v2
	v_exp_f32_e32 v3, v3
	v_and_b32_e32 v4, 0xffff0000, v5
	v_cvt_pk_bf16_f32 v5, v34, v35
	v_add_f32_e32 v3, 1.0, v3
	v_rcp_f32_e32 v3, v3
	s_nop 0
	v_mul_f32_e32 v20, v2, v3
	v_and_b32_e32 v3, 0xffff0000, v21
	v_and_b32_e32 v2, 0xffff0000, v9
	v_pk_mul_f32 v[2:3], v[52:53], v[2:3]
	s_nop 0
	v_fma_f32 v2, v49, v4, v2
	v_add_f32_e32 v2, v2, v3
	v_mul_f32_e32 v3, 0xbfb8aa3b, v2
	v_exp_f32_e32 v3, v3
	v_cvt_pk_bf16_f32 v4, v66, v36
	s_nop 0
	v_add_f32_e32 v3, 1.0, v3
	v_rcp_f32_e32 v3, v3
	s_nop 0
	v_mul_f32_e32 v9, v2, v3
	v_cvt_pk_bf16_f32 v2, v91, v38
	v_cvt_pk_bf16_f32 v3, v78, v39
	v_cvt_pk_bf16_f32 v9, v20, v9
	ds_write_b128 v90, v[2:5] offset:18432
	ds_write_b128 v90, v[6:9] offset:18448
	v_ashrrev_i32_e32 v2, 1, v110
	v_and_b32_e32 v2, -2, v2
	v_add3_u32 v1, 0, v1, v2
	v_lshl_add_u64 v[2:3], s[20:21], 0, v[162:163]
	v_lshl_add_u64 v[4:5], s[90:91], 0, v[158:159]
	v_lshlrev_b64 v[2:3], 7, v[2:3]
	v_lshl_add_u64 v[160:161], v[4:5], 0, v[2:3]
	v_add_co_u32_e32 v2, vcc, s4, v160
	ds_write_b16 v1, v26 offset:36864
	ds_write_b16_d16_hi v1, v26 offset:37136
	ds_write_b16 v1, v27 offset:37408
	ds_write_b16_d16_hi v1, v27 offset:37680
	ds_write_b16 v1, v28 offset:37952
; #define LAS __attribute__((address_space(3)))
; __device__ __forceinline__ float shfl_up_l(float v, int off, int lane) { return __int_as_float(__builtin_amdgcn_ds_bpermute(((lane - off) & 63) << 2, __float_as_int(v))); }
; __device__ __forceinline__ float shfl_l(float v, int src) { return __int_as_float(__builtin_amdgcn_ds_bpermute(src << 2, __float_as_int(v))); }
; __device__ __forceinline__ void gate_scan(const LAS float* li, LAS float* lf, int dir, int lane, int (&pos)[2], float (&b)[2], float (&x)[2], float& g) {
;     pos[0] = dir ? 127 - 2 * lane : 2 * lane; pos[1] = dir ? 126 - 2 * lane : 2 * lane + 1;
;     const float f0 = lf[pos[0]], f1 = lf[pos[1]]; const float s1 = f0 + f1; float inc = s1;
; #pragma unroll
;     for (int off = 1; off < 64; off <<= 1) { const float y = shfl_up_l(inc, off, lane); if (lane >= off) inc += y; }
;     const float exc = inc - s1; b[0] = exc + f0; b[1] = exc + s1; g = shfl_l(inc, 63);
;     lf[pos[0]] = b[0]; lf[pos[1]] = b[1];
;     x[0] = li[pos[0]] - b[0]; x[1] = li[pos[1]] - b[1];
; }
; __device__ __forceinline__ void m3_unit(LAS unsigned char* L, int u, const bf16* z, const float* gates, const float* cw, const bf16* cprev, const float* nprev, const float* mprev, const float* normg, bf16* mix, int tid_) {
;     ...
;     vT_store(L + VT, vr, tid);
;     bf16x8 cpf[8][2];
; #pragma unroll
;     for (int nt = 0; nt < 8; ++nt)
; #pragma unroll
;         for (int ks = 0; ks < 2; ++ks) cpf[nt][ks] = *(const bf16x8*)(cprev + ((size_t)u * 128 + nt * 16 + fr) * 64 + ks * 32 + fq * 8);
;     f32x4 npv = *(const f32x4*)(nprev + (size_t)u * 64 + fr * 4); const float mp0 = mprev[u], mp1 = mprev[512 + u];
;     __syncthreads();
;     if (w < 2) {
;         const int dir = w; LAS float* li = ga + dir * 384; LAS float* lf = li + 128; LAS float* pm = li + 256;
;         int pos[2]; float bq[2], xq[2], g; gate_scan(li, lf, dir, lane, pos, bq, xq, g);
;         const float m1 = fmaxf(xq[0], xq[1]); float inc = m1;
; #pragma unroll
;         for (int off = 1; off < 64; off <<= 1) { const float y = shfl_up_l(inc, off, lane); if (lane >= off) inc = fmaxf(inc, y); }
;         float exc = shfl_up_l(inc, 1, lane); if (lane == 0) exc = -3.0e38f;
;         pm[pos[0]] = fmaxf(exc, xq[0]); pm[pos[1]] = fmaxf(exc, m1);
	ds_write_b16_d16_hi v1, v28 offset:38224
	ds_write_b16 v1, v29 offset:38496
	ds_write_b16_d16_hi v1, v29 offset:38768
	ds_write_b16 v1, v22 offset:39040
	ds_write_b16_d16_hi v1, v22 offset:39312
	ds_write_b16 v1, v23 offset:39584
	ds_write_b16_d16_hi v1, v23 offset:39856
	ds_write_b16 v1, v24 offset:40128
	ds_write_b16_d16_hi v1, v24 offset:40400
	ds_write_b16 v1, v25 offset:40672
	ds_write_b16_d16_hi v1, v25 offset:40944
	ds_write_b16 v1, v14 offset:41216
	ds_write_b16_d16_hi v1, v14 offset:41488
	ds_write_b16 v1, v15 offset:41760
	ds_write_b16_d16_hi v1, v15 offset:42032
	ds_write_b16 v1, v16 offset:42304
	ds_write_b16_d16_hi v1, v16 offset:42576
	ds_write_b16 v1, v17 offset:42848
	ds_write_b16_d16_hi v1, v17 offset:43120
	ds_write_b16 v1, v10 offset:43392
	ds_write_b16_d16_hi v1, v10 offset:43664
	ds_write_b16 v1, v11 offset:43936
	ds_write_b16_d16_hi v1, v11 offset:44208
	ds_write_b16 v1, v12 offset:44480
	ds_write_b16_d16_hi v1, v12 offset:44752
	ds_write_b16 v1, v13 offset:45024
	ds_write_b16_d16_hi v1, v13 offset:45296
	v_addc_co_u32_e32 v3, vcc, 0, v161, vcc
	v_add_co_u32_e32 v4, vcc, s62, v160
	s_movk_i32 s4, 0x3000
	s_nop 0
	v_addc_co_u32_e32 v5, vcc, 0, v161, vcc
	global_load_dwordx4 v[106:109], v[160:161], off
	global_load_dwordx4 v[102:105], v[160:161], off offset:64
	global_load_dwordx4 v[98:101], v[160:161], off offset:2048
	global_load_dwordx4 v[94:97], v[160:161], off offset:2112
	global_load_dwordx4 v[90:93], v[4:5], off offset:-4096
	global_load_dwordx4 v[86:89], v[2:3], off offset:64
	global_load_dwordx4 v[82:85], v[2:3], off offset:2048
	global_load_dwordx4 v[78:81], v[2:3], off offset:2112
	global_load_dwordx4 v[74:77], v[4:5], off
	global_load_dwordx4 v[50:53], v[4:5], off offset:64
	global_load_dwordx4 v[46:49], v[4:5], off offset:2048
	global_load_dwordx4 v[26:29], v[4:5], off offset:2112
	v_add_co_u32_e32 v2, vcc, s4, v160
	s_add_u32 s4, s64, s28
	s_nop 0
	v_addc_co_u32_e32 v3, vcc, 0, v161, vcc
	global_load_dwordx4 v[38:41], v[2:3], off
	global_load_dwordx4 v[42:45], v[2:3], off offset:64
	global_load_dwordx4 v[30:33], v[2:3], off offset:2048
	global_load_dwordx4 v[34:37], v[2:3], off offset:2112
	v_lshlrev_b32_e32 v2, 4, v162
	v_mov_b32_e32 v3, v163
	s_addc_u32 s5, s65, s29
	v_lshl_add_u64 v[168:169], s[4:5], 0, v[2:3]
	s_mov_b32 s4, 0x58740000
	v_add_co_u32_e32 v2, vcc, s4, v168
	s_add_u32 s4, s64, s30
	s_nop 0
	v_addc_co_u32_e32 v3, vcc, 0, v169, vcc
	s_addc_u32 s5, s65, s31
	global_load_dwordx4 v[18:21], v[2:3], off
	global_load_dword v115, v198, s[4:5]
	global_load_dword v184, v198, s[4:5] offset:2048
	v_cmp_gt_i32_e32 vcc, 2, v111
	s_waitcnt lgkmcnt(0)
	s_barrier
	s_and_saveexec_b64 s[8:9], vcc
	s_cbranch_execz .LBB0_787
	v_lshlrev_b32_e32 v2, 1, v119
	s_movk_i32 s4, 0x600
	v_cmp_gt_u32_e32 vcc, 64, v110
	v_xor_b32_e32 v3, 0x7f, v2
	v_mul_lo_u32 v1, v111, s4
	s_add_i32 s4, 0, 0x1a000
	v_cndmask_b32_e32 v3, v3, v2, vcc
	v_xor_b32_e32 v4, 0x7e, v2
	v_or_b32_e32 v2, 1, v2
	v_add_u32_e32 v1, s4, v1
	v_cndmask_b32_e32 v4, v4, v2, vcc
	v_lshl_add_u32 v6, v3, 2, v1
	v_lshl_add_u32 v1, v4, 2, v1
	ds_read2st64_b32 v[2:3], v6 offset1:2
	ds_read2st64_b32 v[4:5], v1 offset1:2
	v_lshlrev_b32_e32 v7, 2, v119
	v_add_u32_e32 v8, 0xfc, v7
	v_and_b32_e32 v8, 0xfc, v8
	v_cmp_eq_u32_e32 vcc, 0, v119
	s_waitcnt lgkmcnt(0)
	v_add_f32_e32 v5, v3, v5
	v_mov_b32_e32 v7, v5
	s_nop 1
	v_add_f32_dpp v7, v7, v7 row_shr:1 row_mask:0xf bank_mask:0xf
	s_nop 1
	v_add_f32_dpp v7, v7, v7 row_shr:2 row_mask:0xf bank_mask:0xf
	s_nop 1
	v_add_f32_dpp v7, v7, v7 row_shr:4 row_mask:0xf bank_mask:0xf
	s_nop 1
	v_add_f32_dpp v7, v7, v7 row_shr:8 row_mask:0xf bank_mask:0xf
	s_nop 1
	v_add_f32_dpp v7, v7, v7 row_bcast:15 row_mask:0xa bank_mask:0xf
	s_nop 1
	v_add_f32_dpp v7, v7, v7 row_bcast:31 row_mask:0xc bank_mask:0xf
	v_sub_f32_e32 v7, v7, v5
	v_add_f32_e32 v3, v3, v7
	v_add_f32_e32 v5, v5, v7
	v_lshlrev_b32_e32 v7, 2, v110
	v_sub_f32_e32 v2, v2, v3
	v_sub_f32_e32 v4, v4, v5
	v_add_u32_e32 v9, 0xfc, v7
	v_max_f32_e32 v4, v2, v4
	v_and_b32_e32 v9, 0xfc, v9
	v_mov_b32_e32 v7, v4
	s_nop 1
	v_max_f32_dpp v7, v7, v7 row_shr:1 row_mask:0xf bank_mask:0xf
	s_nop 1
	v_max_f32_dpp v7, v7, v7 row_shr:2 row_mask:0xf bank_mask:0xf
	s_nop 1
	v_max_f32_dpp v7, v7, v7 row_shr:4 row_mask:0xf bank_mask:0xf
	s_nop 1
	v_max_f32_dpp v7, v7, v7 row_shr:8 row_mask:0xf bank_mask:0xf
	s_nop 1
	v_max_f32_dpp v7, v7, v7 row_bcast:15 row_mask:0xa bank_mask:0xf
	s_nop 1
	v_max_f32_dpp v7, v7, v7 row_bcast:31 row_mask:0xc bank_mask:0xf
	ds_bpermute_b32 v7, v8, v7
	v_mov_b32_e32 v8, 0xff61b1e6
	s_waitcnt lgkmcnt(0)
	v_cndmask_b32_e32 v7, v7, v8, vcc
	v_max_f32_e32 v7, v7, v7
	v_max_f32_e32 v2, v7, v2
	ds_write2st64_b32 v6, v3, v2 offset0:2 offset1:4
	v_max_f32_e32 v2, v7, v4
	ds_write2st64_b32 v1, v5, v2 offset0:2 offset1:4
	s_branch .LBB0_787
